# v69 + P4 bisection step: scalar loop control, one accumulator, DPP add-reduction instead of six bit-sliced ballots (88 vs 111 instructions per step)
# speedup vs baseline: 1.0115x; 1.0040x over previous
; #define SEL_ROW(idx, row, nv) const int bb_ = (idx) >> 11; int t_ = (idx) & 2047; if (bb_ & 1) t_ = 2047 - t_; const size_t row = (size_t)bb_ * SEQ + t_; const int nv = (t_ >> 6) + 1;
; __device__ __forceinline__ void ph4b_body(const Args& a, int wave, int lane, int G, int bid) {
;     ...
;         SEL_ROW(idx, row, nv)
; #pragma unroll
;         for (int i = 0; i < 32; ++i) { const unsigned uu = __float_as_uint(raw[i]); const unsigned kk = (uu & 0x80000000u) ? ~uu : (uu | 0x80000000u); key[i] = (i < nv) ? kk : 0u; }
;         if (idx + NGW < T) { SEL_ROW(idx + NGW, rown, nvn) const float* sp = SC + rown * 2048 + lane;
; #pragma unroll
;             for (int i = 0; i < 32; ++i) raw[i] = __builtin_nontemporal_load(sp + 64 * (i < nvn ? i : nvn - 1)); }
;         unsigned Tt = 0u;
;         if (nv > 4) { if (nv <= 8) Tt = sel_thr<8>(key); else if (nv <= 16) Tt = sel_thr<16>(key); else if (nv <= 24) Tt = sel_thr<24>(key); else Tt = sel_thr<32>(key); }
.LBB0_700:
	s_and_b32 s0, s33, 0x7ff
	v_not_b32_e32 v5, v66
	v_cmp_gt_i32_e32 vcc, 0, v66
	s_and_b32 s1, s33, 0x800
	s_xor_b32 s2, s0, 0x7ff
	v_cndmask_b32_e64 v5, -|v66|, v5, vcc
	v_not_b32_e32 v66, v36
	v_cmp_gt_i32_e32 vcc, 0, v36
	s_cmp_eq_u32 s1, 0
	s_cselect_b32 s34, s0, s2
	v_cndmask_b32_e64 v36, -|v36|, v66, vcc
	v_not_b32_e32 v66, v37
	v_cmp_gt_i32_e32 vcc, 0, v37
	s_lshr_b32 s38, s34, 6
	s_cmpk_gt_u32 s34, 0x13f
	v_cndmask_b32_e64 v37, -|v37|, v66, vcc
	v_not_b32_e32 v66, v38
	v_cmp_gt_i32_e32 vcc, 0, v38
	s_nop 1
	v_cndmask_b32_e64 v38, -|v38|, v66, vcc
	v_not_b32_e32 v66, v39
	v_cmp_gt_i32_e32 vcc, 0, v39
	s_nop 1
	v_cndmask_b32_e64 v39, -|v39|, v66, vcc
	v_not_b32_e32 v66, v35
	v_cmp_gt_i32_e32 vcc, 0, v35
	s_nop 1
	v_cndmask_b32_e64 v67, -|v35|, v66, vcc
	s_cselect_b64 vcc, -1, 0
	v_cndmask_b32_e32 v35, 0, v67, vcc
	v_not_b32_e32 v66, v40
	v_cmp_gt_i32_e32 vcc, 0, v40
	s_cmpk_gt_u32 s34, 0x17f
	s_nop 0
	v_cndmask_b32_e64 v68, -|v40|, v66, vcc
	s_cselect_b64 vcc, -1, 0
	v_cndmask_b32_e32 v40, 0, v68, vcc
	v_not_b32_e32 v66, v41
	v_cmp_gt_i32_e32 vcc, 0, v41
	s_cmpk_gt_u32 s34, 0x1bf
	s_nop 0
	v_cndmask_b32_e64 v69, -|v41|, v66, vcc
	s_cselect_b64 vcc, -1, 0
	s_cmpk_lt_u32 s34, 0x200
	v_cndmask_b32_e32 v41, 0, v69, vcc
	v_not_b32_e32 v66, v43
	v_cmp_gt_i32_e32 vcc, 0, v43
	s_cselect_b64 s[0:1], -1, 0
	s_cmpk_gt_u32 s34, 0x1ff
	v_cndmask_b32_e64 v43, -|v43|, v66, vcc
	s_cselect_b64 s[6:7], -1, 0
	v_not_b32_e32 v66, v42
	v_cmp_gt_i32_e32 vcc, 0, v42
	s_cmpk_gt_u32 s34, 0x23f
	s_nop 0
	v_cndmask_b32_e64 v70, -|v42|, v66, vcc
	s_cselect_b64 vcc, -1, 0
	v_cndmask_b32_e32 v42, 0, v70, vcc
	v_not_b32_e32 v66, v44
	v_cmp_gt_i32_e32 vcc, 0, v44
	s_cmpk_gt_u32 s34, 0x27f
	s_nop 0
	v_cndmask_b32_e64 v71, -|v44|, v66, vcc
	s_cselect_b64 vcc, -1, 0
	v_cndmask_b32_e32 v44, 0, v71, vcc
	v_not_b32_e32 v66, v45
	v_cmp_gt_i32_e32 vcc, 0, v45
	s_cmpk_gt_u32 s34, 0x2bf
	s_nop 0
	v_cndmask_b32_e64 v72, -|v45|, v66, vcc
	s_cselect_b64 vcc, -1, 0
	v_cndmask_b32_e32 v45, 0, v72, vcc
	v_not_b32_e32 v66, v46
	v_cmp_gt_i32_e32 vcc, 0, v46
	s_cmpk_gt_u32 s34, 0x2ff
	s_nop 0
	v_cndmask_b32_e64 v73, -|v46|, v66, vcc
	s_cselect_b64 vcc, -1, 0
	v_cndmask_b32_e32 v46, 0, v73, vcc
	v_not_b32_e32 v66, v47
	v_cmp_gt_i32_e32 vcc, 0, v47
	s_cmpk_gt_u32 s34, 0x33f
	s_nop 0
	v_cndmask_b32_e64 v74, -|v47|, v66, vcc
	s_cselect_b64 vcc, -1, 0
	v_cndmask_b32_e32 v47, 0, v74, vcc
	v_not_b32_e32 v66, v48
	v_cmp_gt_i32_e32 vcc, 0, v48
	s_cmpk_gt_u32 s34, 0x37f
	s_nop 0
	v_cndmask_b32_e64 v75, -|v48|, v66, vcc
	s_cselect_b64 vcc, -1, 0
	v_cndmask_b32_e32 v48, 0, v75, vcc
	v_not_b32_e32 v66, v49
	v_cmp_gt_i32_e32 vcc, 0, v49
	s_cmpk_gt_u32 s34, 0x3bf
	s_nop 0
	v_cndmask_b32_e64 v76, -|v49|, v66, vcc
	s_cselect_b64 vcc, -1, 0
	s_cmpk_lt_u32 s34, 0x400
	v_cndmask_b32_e32 v49, 0, v76, vcc
	v_not_b32_e32 v66, v52
	v_cmp_gt_i32_e32 vcc, 0, v52
	s_cselect_b64 s[2:3], -1, 0
	s_cmpk_gt_u32 s34, 0x3ff
	v_cndmask_b32_e64 v52, -|v52|, v66, vcc
	s_cselect_b64 s[8:9], -1, 0
	v_not_b32_e32 v66, v50
	v_cmp_gt_i32_e32 vcc, 0, v50
	s_cmpk_gt_u32 s34, 0x43f
	s_nop 0
	v_cndmask_b32_e64 v77, -|v50|, v66, vcc
	s_cselect_b64 vcc, -1, 0
	v_cndmask_b32_e32 v50, 0, v77, vcc
	v_not_b32_e32 v66, v51
	v_cmp_gt_i32_e32 vcc, 0, v51
	s_cmpk_gt_u32 s34, 0x47f
	s_nop 0
	v_cndmask_b32_e64 v78, -|v51|, v66, vcc
	s_cselect_b64 vcc, -1, 0
	v_cndmask_b32_e32 v51, 0, v78, vcc
	v_not_b32_e32 v66, v53
	v_cmp_gt_i32_e32 vcc, 0, v53
	s_cmpk_gt_u32 s34, 0x4bf
	s_nop 0
	v_cndmask_b32_e64 v79, -|v53|, v66, vcc
	s_cselect_b64 vcc, -1, 0
	v_cndmask_b32_e32 v53, 0, v79, vcc
	v_not_b32_e32 v66, v54
	v_cmp_gt_i32_e32 vcc, 0, v54
	s_cmpk_gt_u32 s34, 0x4ff
	s_nop 0
	v_cndmask_b32_e64 v80, -|v54|, v66, vcc
	s_cselect_b64 vcc, -1, 0
	v_cndmask_b32_e32 v54, 0, v80, vcc
	v_not_b32_e32 v66, v55
	v_cmp_gt_i32_e32 vcc, 0, v55
	s_cmpk_gt_u32 s34, 0x53f
	s_nop 0
	v_cndmask_b32_e64 v81, -|v55|, v66, vcc
	s_cselect_b64 vcc, -1, 0
	v_cndmask_b32_e32 v55, 0, v81, vcc
	v_not_b32_e32 v66, v56
	v_cmp_gt_i32_e32 vcc, 0, v56
	s_cmpk_gt_u32 s34, 0x57f
	s_nop 0
	v_cndmask_b32_e64 v82, -|v56|, v66, vcc
	s_cselect_b64 vcc, -1, 0
	v_cndmask_b32_e32 v56, 0, v82, vcc
	v_not_b32_e32 v66, v57
	v_cmp_gt_i32_e32 vcc, 0, v57
	s_cmpk_gt_u32 s34, 0x5bf
	s_nop 0
	v_cndmask_b32_e64 v83, -|v57|, v66, vcc
	s_cselect_b64 vcc, -1, 0
	s_cmpk_lt_u32 s34, 0x600
	v_cndmask_b32_e32 v57, 0, v83, vcc
	v_not_b32_e32 v66, v62
	v_cmp_gt_i32_e32 vcc, 0, v62
	s_cselect_b64 s[4:5], -1, 0
	s_cmpk_gt_u32 s34, 0x5ff
	v_cndmask_b32_e64 v62, -|v62|, v66, vcc
	s_cselect_b64 s[10:11], -1, 0
	v_not_b32_e32 v66, v58
	v_cmp_gt_i32_e32 vcc, 0, v58
	s_cmpk_gt_u32 s34, 0x63f
	s_nop 0
	v_cndmask_b32_e64 v58, -|v58|, v66, vcc
	s_cselect_b64 vcc, -1, 0
	v_cndmask_b32_e32 v58, 0, v58, vcc
	v_not_b32_e32 v66, v59
	v_cmp_gt_i32_e32 vcc, 0, v59
	s_cmpk_gt_u32 s34, 0x67f
	s_nop 0
	v_cndmask_b32_e64 v59, -|v59|, v66, vcc
	s_cselect_b64 vcc, -1, 0
	v_cndmask_b32_e32 v59, 0, v59, vcc
	v_not_b32_e32 v66, v60
	v_cmp_gt_i32_e32 vcc, 0, v60
	s_cmpk_gt_u32 s34, 0x6bf
	s_nop 0
	v_cndmask_b32_e64 v60, -|v60|, v66, vcc
	s_cselect_b64 vcc, -1, 0
	v_cndmask_b32_e32 v60, 0, v60, vcc
	v_not_b32_e32 v66, v61
	v_cmp_gt_i32_e32 vcc, 0, v61
	s_cmpk_gt_u32 s34, 0x6ff
	s_nop 0
	v_cndmask_b32_e64 v61, -|v61|, v66, vcc
	s_cselect_b64 vcc, -1, 0
	v_cndmask_b32_e32 v61, 0, v61, vcc
	v_not_b32_e32 v66, v63
	v_cmp_gt_i32_e32 vcc, 0, v63
	s_cmpk_gt_u32 s34, 0x73f
	s_nop 0
	v_cndmask_b32_e64 v63, -|v63|, v66, vcc
	s_cselect_b64 vcc, -1, 0
	v_cndmask_b32_e32 v63, 0, v63, vcc
	v_not_b32_e32 v66, v64
	v_cmp_gt_i32_e32 vcc, 0, v64
	s_cmpk_gt_u32 s34, 0x77f
	s_nop 0
	v_cndmask_b32_e64 v64, -|v64|, v66, vcc
	s_cselect_b64 vcc, -1, 0
	v_cndmask_b32_e32 v64, 0, v64, vcc
	v_not_b32_e32 v66, v65
	v_cmp_gt_i32_e32 vcc, 0, v65
	s_cmp_eq_u32 s38, 31
	s_nop 0
	v_cndmask_b32_e64 v65, -|v65|, v66, vcc
	s_cselect_b64 vcc, -1, 0
	v_cndmask_b32_e32 v65, 0, v65, vcc
	s_cmpk_lt_u32 s34, 0x100
	v_mov_b32_e32 v66, 0
	s_cbranch_scc1 .LBB0_718
	s_and_b64 vcc, exec, s[6:7]
	s_cbranch_vccz .LBB0_707
	s_and_b64 vcc, exec, s[8:9]
	s_cbranch_vccz .LBB0_708
	s_andn2_b64 vcc, exec, s[10:11]
	s_cbranch_vccnz .LBB0_709
	v_mov_b32_e32 v84, 31
	v_mov_b32_e32 v66, 0
	s_mov_b32 s26, 31
	s_mov_b32 s28, 0
; template <int NVM> __device__ __forceinline__ int cnt_ge(const unsigned (&key)[32], unsigned cand) {
;     unsigned c0 = 0, c1 = 0, c2 = 0, c3 = 0;
; #pragma unroll
;     for (int i = 0; i < NVM; i += 4) {
;         asm("v_cmp_ge_u32 vcc, %1, %2\n\tv_addc_co_u32 %0, vcc, 0, %0, vcc" : "+v"(c0) : "v"(key[i]), "v"(cand) : "vcc");
;         asm("v_cmp_ge_u32 vcc, %1, %2\n\tv_addc_co_u32 %0, vcc, 0, %0, vcc" : "+v"(c1) : "v"(key[i + 1]), "v"(cand) : "vcc");
;         asm("v_cmp_ge_u32 vcc, %1, %2\n\tv_addc_co_u32 %0, vcc, 0, %0, vcc" : "+v"(c2) : "v"(key[i + 2]), "v"(cand) : "vcc");
;         asm("v_cmp_ge_u32 vcc, %1, %2\n\tv_addc_co_u32 %0, vcc, 0, %0, vcc" : "+v"(c3) : "v"(key[i + 3]), "v"(cand) : "vcc"); }
;     const unsigned c = (c0 + c1) + (c2 + c3);
;     int tot = 0;
; #pragma unroll
;     for (int b = 0; b < 6; ++b) tot += __builtin_popcountll(__ballot((c >> b) & 1u)) << b;
;     return tot;
; }
; template <int NVM> __device__ __forceinline__ unsigned sel_thr(const unsigned (&key)[32]) {
;     unsigned Tt = 0u;
;     ...
;         if (cnt >= TOPK) { Tt = cand; if (cnt == TOPK) break; } }
;     return Tt;
; }
.LBB0_705:
	s_lshl_b32 s27, 1, s26
	s_or_b32 s27, s27, s28
	v_mov_b32_e32 v86, 0
	v_cmp_le_u32_e32 vcc, s27, v5
	v_addc_co_u32_e32 v86, vcc, 0, v86, vcc
	v_cmp_le_u32_e32 vcc, s27, v36
	v_addc_co_u32_e32 v86, vcc, 0, v86, vcc
	v_cmp_le_u32_e32 vcc, s27, v39
	v_addc_co_u32_e32 v86, vcc, 0, v86, vcc
	v_cmp_le_u32_e32 vcc, s27, v37
	v_addc_co_u32_e32 v86, vcc, 0, v86, vcc
	v_cmp_le_u32_e32 vcc, s27, v38
	v_addc_co_u32_e32 v86, vcc, 0, v86, vcc
	v_cmp_le_u32_e32 vcc, s27, v67
	v_addc_co_u32_e32 v86, vcc, 0, v86, vcc
	v_cmp_le_u32_e32 vcc, s27, v43
	v_addc_co_u32_e32 v86, vcc, 0, v86, vcc
	v_cmp_le_u32_e32 vcc, s27, v68
	v_addc_co_u32_e32 v86, vcc, 0, v86, vcc
	v_cmp_le_u32_e32 vcc, s27, v69
	v_addc_co_u32_e32 v86, vcc, 0, v86, vcc
	v_cmp_le_u32_e32 vcc, s27, v70
	v_addc_co_u32_e32 v86, vcc, 0, v86, vcc
	v_cmp_le_u32_e32 vcc, s27, v73
	v_addc_co_u32_e32 v86, vcc, 0, v86, vcc
	v_cmp_le_u32_e32 vcc, s27, v71
	v_addc_co_u32_e32 v86, vcc, 0, v86, vcc
	v_cmp_le_u32_e32 vcc, s27, v72
	v_addc_co_u32_e32 v86, vcc, 0, v86, vcc
	v_cmp_le_u32_e32 vcc, s27, v74
	v_addc_co_u32_e32 v86, vcc, 0, v86, vcc
	v_cmp_le_u32_e32 vcc, s27, v52
	v_addc_co_u32_e32 v86, vcc, 0, v86, vcc
	v_cmp_le_u32_e32 vcc, s27, v75
	v_addc_co_u32_e32 v86, vcc, 0, v86, vcc
	v_cmp_le_u32_e32 vcc, s27, v76
	v_addc_co_u32_e32 v86, vcc, 0, v86, vcc
	v_cmp_le_u32_e32 vcc, s27, v77
	v_addc_co_u32_e32 v86, vcc, 0, v86, vcc
	v_cmp_le_u32_e32 vcc, s27, v80
	v_addc_co_u32_e32 v86, vcc, 0, v86, vcc
	v_cmp_le_u32_e32 vcc, s27, v78
	v_addc_co_u32_e32 v86, vcc, 0, v86, vcc
	v_cmp_le_u32_e32 vcc, s27, v79
	v_addc_co_u32_e32 v86, vcc, 0, v86, vcc
	v_cmp_le_u32_e32 vcc, s27, v81
	v_addc_co_u32_e32 v86, vcc, 0, v86, vcc
	v_cmp_le_u32_e32 vcc, s27, v62
	v_addc_co_u32_e32 v86, vcc, 0, v86, vcc
	v_cmp_le_u32_e32 vcc, s27, v82
	v_addc_co_u32_e32 v86, vcc, 0, v86, vcc
	v_cmp_le_u32_e32 vcc, s27, v83
	v_addc_co_u32_e32 v86, vcc, 0, v86, vcc
	v_cmp_le_u32_e32 vcc, s27, v58
	v_addc_co_u32_e32 v86, vcc, 0, v86, vcc
	v_cmp_le_u32_e32 vcc, s27, v61
	v_addc_co_u32_e32 v86, vcc, 0, v86, vcc
	v_cmp_le_u32_e32 vcc, s27, v59
	v_addc_co_u32_e32 v86, vcc, 0, v86, vcc
	v_cmp_le_u32_e32 vcc, s27, v60
	v_addc_co_u32_e32 v86, vcc, 0, v86, vcc
	v_cmp_le_u32_e32 vcc, s27, v63
	v_addc_co_u32_e32 v86, vcc, 0, v86, vcc
	v_cmp_le_u32_e32 vcc, s27, v64
	v_addc_co_u32_e32 v86, vcc, 0, v86, vcc
	v_cmp_le_u32_e32 vcc, s27, v65
	v_addc_co_u32_e32 v86, vcc, 0, v86, vcc
	s_nop 1
	v_add_u32_dpp v86, v86, v86 quad_perm:[1,0,3,2] row_mask:0xf bank_mask:0xf
	s_nop 1
	v_add_u32_dpp v86, v86, v86 quad_perm:[2,3,0,1] row_mask:0xf bank_mask:0xf
	s_nop 1
	v_add_u32_dpp v86, v86, v86 row_ror:4 row_mask:0xf bank_mask:0xf
	s_nop 1
	v_add_u32_dpp v86, v86, v86 row_ror:8 row_mask:0xf bank_mask:0xf
	s_nop 1
	v_add_u32_dpp v86, v86, v86 row_bcast:15 row_mask:0xa bank_mask:0xf
	s_nop 1
	v_add_u32_dpp v86, v86, v86 row_bcast:31 row_mask:0xc bank_mask:0xf
	s_nop 1
	v_readlane_b32 s12, v86, 63
	s_cmpk_ge_u32 s12, 0x100
	s_cselect_b32 s28, s27, s28
	s_cmpk_eq_u32 s12, 0x100
	s_cbranch_scc1 .Lp4d_705
	s_add_i32 s26, s26, -1
	s_cmp_ge_i32 s26, 0
	s_cbranch_scc1 .LBB0_705
.Lp4d_705:
	v_mov_b32_e32 v66, s28
	s_branch .LBB0_712

; template <int NVM> __device__ __forceinline__ int cnt_ge(const unsigned (&key)[32], unsigned cand) {
;     unsigned c0 = 0, c1 = 0, c2 = 0, c3 = 0;
; #pragma unroll
;     for (int i = 0; i < NVM; i += 4) {
;         asm("v_cmp_ge_u32 vcc, %1, %2\n\tv_addc_co_u32 %0, vcc, 0, %0, vcc" : "+v"(c0) : "v"(key[i]), "v"(cand) : "vcc");
;         asm("v_cmp_ge_u32 vcc, %1, %2\n\tv_addc_co_u32 %0, vcc, 0, %0, vcc" : "+v"(c1) : "v"(key[i + 1]), "v"(cand) : "vcc");
;         asm("v_cmp_ge_u32 vcc, %1, %2\n\tv_addc_co_u32 %0, vcc, 0, %0, vcc" : "+v"(c2) : "v"(key[i + 2]), "v"(cand) : "vcc");
;         asm("v_cmp_ge_u32 vcc, %1, %2\n\tv_addc_co_u32 %0, vcc, 0, %0, vcc" : "+v"(c3) : "v"(key[i + 3]), "v"(cand) : "vcc"); }
;     const unsigned c = (c0 + c1) + (c2 + c3);
;     int tot = 0;
; #pragma unroll
;     for (int b = 0; b < 6; ++b) tot += __builtin_popcountll(__ballot((c >> b) & 1u)) << b;
;     return tot;
; }
; template <int NVM> __device__ __forceinline__ unsigned sel_thr(const unsigned (&key)[32]) {
;     unsigned Tt = 0u;
;     ...
;         if (cnt >= TOPK) { Tt = cand; if (cnt == TOPK) break; } }
;     return Tt;
; }
.LBB0_709:
	s_cbranch_execz .LBB0_712
	v_mov_b32_e32 v77, 31
	v_mov_b32_e32 v66, 0
	s_mov_b32 s26, 31
	s_mov_b32 s28, 0
.LBB0_711:
	s_lshl_b32 s27, 1, s26
	s_or_b32 s27, s27, s28
	v_mov_b32_e32 v79, 0
	v_cmp_le_u32_e32 vcc, s27, v5
	v_addc_co_u32_e32 v79, vcc, 0, v79, vcc
	v_cmp_le_u32_e32 vcc, s27, v36
	v_addc_co_u32_e32 v79, vcc, 0, v79, vcc
	v_cmp_le_u32_e32 vcc, s27, v39
	v_addc_co_u32_e32 v79, vcc, 0, v79, vcc
	v_cmp_le_u32_e32 vcc, s27, v37
	v_addc_co_u32_e32 v79, vcc, 0, v79, vcc
	v_cmp_le_u32_e32 vcc, s27, v38
	v_addc_co_u32_e32 v79, vcc, 0, v79, vcc
	v_cmp_le_u32_e32 vcc, s27, v67
	v_addc_co_u32_e32 v79, vcc, 0, v79, vcc
	v_cmp_le_u32_e32 vcc, s27, v43
	v_addc_co_u32_e32 v79, vcc, 0, v79, vcc
	v_cmp_le_u32_e32 vcc, s27, v68
	v_addc_co_u32_e32 v79, vcc, 0, v79, vcc
	v_cmp_le_u32_e32 vcc, s27, v69
	v_addc_co_u32_e32 v79, vcc, 0, v79, vcc
	v_cmp_le_u32_e32 vcc, s27, v70
	v_addc_co_u32_e32 v79, vcc, 0, v79, vcc
	v_cmp_le_u32_e32 vcc, s27, v73
	v_addc_co_u32_e32 v79, vcc, 0, v79, vcc
	v_cmp_le_u32_e32 vcc, s27, v71
	v_addc_co_u32_e32 v79, vcc, 0, v79, vcc
	v_cmp_le_u32_e32 vcc, s27, v72
	v_addc_co_u32_e32 v79, vcc, 0, v79, vcc
	v_cmp_le_u32_e32 vcc, s27, v74
	v_addc_co_u32_e32 v79, vcc, 0, v79, vcc
	v_cmp_le_u32_e32 vcc, s27, v52
	v_addc_co_u32_e32 v79, vcc, 0, v79, vcc
	v_cmp_le_u32_e32 vcc, s27, v75
	v_addc_co_u32_e32 v79, vcc, 0, v79, vcc
	v_cmp_le_u32_e32 vcc, s27, v76
	v_addc_co_u32_e32 v79, vcc, 0, v79, vcc
	v_cmp_le_u32_e32 vcc, s27, v50
	v_addc_co_u32_e32 v79, vcc, 0, v79, vcc
	v_cmp_le_u32_e32 vcc, s27, v54
	v_addc_co_u32_e32 v79, vcc, 0, v79, vcc
	v_cmp_le_u32_e32 vcc, s27, v51
	v_addc_co_u32_e32 v79, vcc, 0, v79, vcc
	v_cmp_le_u32_e32 vcc, s27, v53
	v_addc_co_u32_e32 v79, vcc, 0, v79, vcc
	v_cmp_le_u32_e32 vcc, s27, v55
	v_addc_co_u32_e32 v79, vcc, 0, v79, vcc
	v_cmp_le_u32_e32 vcc, s27, v56
	v_addc_co_u32_e32 v79, vcc, 0, v79, vcc
	v_cmp_le_u32_e32 vcc, s27, v57
	v_addc_co_u32_e32 v79, vcc, 0, v79, vcc
	s_nop 1
	v_add_u32_dpp v79, v79, v79 quad_perm:[1,0,3,2] row_mask:0xf bank_mask:0xf
	s_nop 1
	v_add_u32_dpp v79, v79, v79 quad_perm:[2,3,0,1] row_mask:0xf bank_mask:0xf
	s_nop 1
	v_add_u32_dpp v79, v79, v79 row_ror:4 row_mask:0xf bank_mask:0xf
	s_nop 1
	v_add_u32_dpp v79, v79, v79 row_ror:8 row_mask:0xf bank_mask:0xf
	s_nop 1
	v_add_u32_dpp v79, v79, v79 row_bcast:15 row_mask:0xa bank_mask:0xf
	s_nop 1
	v_add_u32_dpp v79, v79, v79 row_bcast:31 row_mask:0xc bank_mask:0xf
	s_nop 1
	v_readlane_b32 s12, v79, 63
	s_cmpk_ge_u32 s12, 0x100
	s_cselect_b32 s28, s27, s28
	s_cmpk_eq_u32 s12, 0x100
	s_cbranch_scc1 .Lp4d_711
	s_add_i32 s26, s26, -1
	s_cmp_ge_i32 s26, 0
	s_cbranch_scc1 .LBB0_711
.Lp4d_711:
	v_mov_b32_e32 v66, s28

; template <int NVM> __device__ __forceinline__ int cnt_ge(const unsigned (&key)[32], unsigned cand) {
;     unsigned c0 = 0, c1 = 0, c2 = 0, c3 = 0;
; #pragma unroll
;     for (int i = 0; i < NVM; i += 4) {
;         asm("v_cmp_ge_u32 vcc, %1, %2\n\tv_addc_co_u32 %0, vcc, 0, %0, vcc" : "+v"(c0) : "v"(key[i]), "v"(cand) : "vcc");
;         asm("v_cmp_ge_u32 vcc, %1, %2\n\tv_addc_co_u32 %0, vcc, 0, %0, vcc" : "+v"(c1) : "v"(key[i + 1]), "v"(cand) : "vcc");
;         asm("v_cmp_ge_u32 vcc, %1, %2\n\tv_addc_co_u32 %0, vcc, 0, %0, vcc" : "+v"(c2) : "v"(key[i + 2]), "v"(cand) : "vcc");
;         asm("v_cmp_ge_u32 vcc, %1, %2\n\tv_addc_co_u32 %0, vcc, 0, %0, vcc" : "+v"(c3) : "v"(key[i + 3]), "v"(cand) : "vcc"); }
;     const unsigned c = (c0 + c1) + (c2 + c3);
;     int tot = 0;
; #pragma unroll
;     for (int b = 0; b < 6; ++b) tot += __builtin_popcountll(__ballot((c >> b) & 1u)) << b;
;     return tot;
; }
; template <int NVM> __device__ __forceinline__ unsigned sel_thr(const unsigned (&key)[32]) {
;     unsigned Tt = 0u;
;     ...
;         if (cnt >= TOPK) { Tt = cand; if (cnt == TOPK) break; } }
;     return Tt;
; }
.LBB0_713:
	v_mov_b32_e32 v70, 31
	v_mov_b32_e32 v66, 0
	s_mov_b32 s26, 31
	s_mov_b32 s28, 0
.LBB0_714:
	s_lshl_b32 s27, 1, s26
	s_or_b32 s27, s27, s28
	v_mov_b32_e32 v72, 0
	v_cmp_le_u32_e32 vcc, s27, v5
	v_addc_co_u32_e32 v72, vcc, 0, v72, vcc
	v_cmp_le_u32_e32 vcc, s27, v36
	v_addc_co_u32_e32 v72, vcc, 0, v72, vcc
	v_cmp_le_u32_e32 vcc, s27, v39
	v_addc_co_u32_e32 v72, vcc, 0, v72, vcc
	v_cmp_le_u32_e32 vcc, s27, v37
	v_addc_co_u32_e32 v72, vcc, 0, v72, vcc
	v_cmp_le_u32_e32 vcc, s27, v38
	v_addc_co_u32_e32 v72, vcc, 0, v72, vcc
	v_cmp_le_u32_e32 vcc, s27, v67
	v_addc_co_u32_e32 v72, vcc, 0, v72, vcc
	v_cmp_le_u32_e32 vcc, s27, v43
	v_addc_co_u32_e32 v72, vcc, 0, v72, vcc
	v_cmp_le_u32_e32 vcc, s27, v68
	v_addc_co_u32_e32 v72, vcc, 0, v72, vcc
	v_cmp_le_u32_e32 vcc, s27, v69
	v_addc_co_u32_e32 v72, vcc, 0, v72, vcc
	v_cmp_le_u32_e32 vcc, s27, v42
	v_addc_co_u32_e32 v72, vcc, 0, v72, vcc
	v_cmp_le_u32_e32 vcc, s27, v46
	v_addc_co_u32_e32 v72, vcc, 0, v72, vcc
	v_cmp_le_u32_e32 vcc, s27, v44
	v_addc_co_u32_e32 v72, vcc, 0, v72, vcc
	v_cmp_le_u32_e32 vcc, s27, v45
	v_addc_co_u32_e32 v72, vcc, 0, v72, vcc
	v_cmp_le_u32_e32 vcc, s27, v47
	v_addc_co_u32_e32 v72, vcc, 0, v72, vcc
	v_cmp_le_u32_e32 vcc, s27, v48
	v_addc_co_u32_e32 v72, vcc, 0, v72, vcc
	v_cmp_le_u32_e32 vcc, s27, v49
	v_addc_co_u32_e32 v72, vcc, 0, v72, vcc
	s_nop 1
	v_add_u32_dpp v72, v72, v72 quad_perm:[1,0,3,2] row_mask:0xf bank_mask:0xf
	s_nop 1
	v_add_u32_dpp v72, v72, v72 quad_perm:[2,3,0,1] row_mask:0xf bank_mask:0xf
	s_nop 1
	v_add_u32_dpp v72, v72, v72 row_ror:4 row_mask:0xf bank_mask:0xf
	s_nop 1
	v_add_u32_dpp v72, v72, v72 row_ror:8 row_mask:0xf bank_mask:0xf
	s_nop 1
	v_add_u32_dpp v72, v72, v72 row_bcast:15 row_mask:0xa bank_mask:0xf
	s_nop 1
	v_add_u32_dpp v72, v72, v72 row_bcast:31 row_mask:0xc bank_mask:0xf
	s_nop 1
	v_readlane_b32 s12, v72, 63
	s_cmpk_ge_u32 s12, 0x100
	s_cselect_b32 s28, s27, s28
	s_cmpk_eq_u32 s12, 0x100
	s_cbranch_scc1 .Lp4d_714
	s_add_i32 s26, s26, -1
	s_cmp_ge_i32 s26, 0
	s_cbranch_scc1 .LBB0_714

; template <int NVM> __device__ __forceinline__ int cnt_ge(const unsigned (&key)[32], unsigned cand) {
;     unsigned c0 = 0, c1 = 0, c2 = 0, c3 = 0;
; #pragma unroll
;     for (int i = 0; i < NVM; i += 4) {
;         asm("v_cmp_ge_u32 vcc, %1, %2\n\tv_addc_co_u32 %0, vcc, 0, %0, vcc" : "+v"(c0) : "v"(key[i]), "v"(cand) : "vcc");
;         asm("v_cmp_ge_u32 vcc, %1, %2\n\tv_addc_co_u32 %0, vcc, 0, %0, vcc" : "+v"(c1) : "v"(key[i + 1]), "v"(cand) : "vcc");
;         asm("v_cmp_ge_u32 vcc, %1, %2\n\tv_addc_co_u32 %0, vcc, 0, %0, vcc" : "+v"(c2) : "v"(key[i + 2]), "v"(cand) : "vcc");
;         asm("v_cmp_ge_u32 vcc, %1, %2\n\tv_addc_co_u32 %0, vcc, 0, %0, vcc" : "+v"(c3) : "v"(key[i + 3]), "v"(cand) : "vcc"); }
;     const unsigned c = (c0 + c1) + (c2 + c3);
;     int tot = 0;
; #pragma unroll
;     for (int b = 0; b < 6; ++b) tot += __builtin_popcountll(__ballot((c >> b) & 1u)) << b;
;     return tot;
; }
; template <int NVM> __device__ __forceinline__ unsigned sel_thr(const unsigned (&key)[32]) {
;     unsigned Tt = 0u;
;     ...
;         if (cnt >= TOPK) { Tt = cand; if (cnt == TOPK) break; } }
;     return Tt;
; }
.LBB0_716:
	v_mov_b32_e32 v67, 31
	v_mov_b32_e32 v66, 0
	s_mov_b32 s26, 31
	s_mov_b32 s28, 0
.LBB0_717:
	s_lshl_b32 s27, 1, s26
	s_or_b32 s27, s27, s28
	v_mov_b32_e32 v69, 0
	v_cmp_le_u32_e32 vcc, s27, v5
	v_addc_co_u32_e32 v69, vcc, 0, v69, vcc
	v_cmp_le_u32_e32 vcc, s27, v36
	v_addc_co_u32_e32 v69, vcc, 0, v69, vcc
	v_cmp_le_u32_e32 vcc, s27, v39
	v_addc_co_u32_e32 v69, vcc, 0, v69, vcc
	v_cmp_le_u32_e32 vcc, s27, v37
	v_addc_co_u32_e32 v69, vcc, 0, v69, vcc
	v_cmp_le_u32_e32 vcc, s27, v38
	v_addc_co_u32_e32 v69, vcc, 0, v69, vcc
	v_cmp_le_u32_e32 vcc, s27, v35
	v_addc_co_u32_e32 v69, vcc, 0, v69, vcc
	v_cmp_le_u32_e32 vcc, s27, v40
	v_addc_co_u32_e32 v69, vcc, 0, v69, vcc
	v_cmp_le_u32_e32 vcc, s27, v41
	v_addc_co_u32_e32 v69, vcc, 0, v69, vcc
	s_nop 1
	v_add_u32_dpp v69, v69, v69 quad_perm:[1,0,3,2] row_mask:0xf bank_mask:0xf
	s_nop 1
	v_add_u32_dpp v69, v69, v69 quad_perm:[2,3,0,1] row_mask:0xf bank_mask:0xf
	s_nop 1
	v_add_u32_dpp v69, v69, v69 row_ror:4 row_mask:0xf bank_mask:0xf
	s_nop 1
	v_add_u32_dpp v69, v69, v69 row_ror:8 row_mask:0xf bank_mask:0xf
	s_nop 1
	v_add_u32_dpp v69, v69, v69 row_bcast:15 row_mask:0xa bank_mask:0xf
	s_nop 1
	v_add_u32_dpp v69, v69, v69 row_bcast:31 row_mask:0xc bank_mask:0xf
	s_nop 1
	v_readlane_b32 s12, v69, 63
	s_cmpk_ge_u32 s12, 0x100
	s_cselect_b32 s28, s27, s28
	s_cmpk_eq_u32 s12, 0x100
	s_cbranch_scc1 .Lp4d_717
	s_add_i32 s26, s26, -1
	s_cmp_ge_i32 s26, 0
	s_cbranch_scc1 .LBB0_717
